# baseline (speedup 1.0000x reference)
_Z6gat_k2PKDF16_S0_S0_PKfPf:
	s_load_dwordx8 s[4:11], s[0:1], 0x0
	s_load_dwordx2 s[12:13], s[0:1], 0x20
	v_readfirstlane_b32 s14, v0
	v_and_b32_e32 v46, 63, v0
	v_lshlrev_b32_e32 v1, 4, v46
	s_and_b32 s16, s2, 1
	s_bfe_u32 s17, s2, 0x60003
	s_lshr_b32 s18, s2, 1
	s_lshr_b32 s15, s14, 6
	s_lshl_b32 s19, s16, 19
	s_lshl_b32 s23, s15, 16
	s_add_u32 s19, s19, s23
	s_lshl_b32 s23, s15, 11
	v_add_u32_e32 v47, s23, v1
	v_and_b32_e32 v44, 31, v0
	v_lshlrev_b32_e32 v45, 2, v44
	s_lshl_b32 s23, s18, 8
	v_add_u32_e32 v45, s23, v45
	s_waitcnt lgkmcnt(0)
	global_load_dword v42, v45, s[10:11]
	global_load_dword v43, v45, s[10:11] offset:128
	global_load_dwordx4 v[48:51], v47, s[6:7]
	global_load_dwordx4 v[52:55], v47, s[6:7] offset:1024
	global_load_dwordx4 v[56:59], v47, s[8:9]
	global_load_dwordx4 v[60:63], v47, s[8:9] offset:1024
	s_add_u32 s20, s4, s19
	s_addc_u32 s21, s5, 0
	s_add_u32 s23, s17, 0
	s_and_b32 s23, s23, 63
	s_lshl_b32 s23, s23, 10
	s_add_u32 s24, s20, s23
	s_addc_u32 s25, s21, 0
	global_load_dwordx4 v[64:67], v1, s[24:25]
	s_add_u32 s23, s17, 1
	s_and_b32 s23, s23, 63
	s_lshl_b32 s23, s23, 10
	s_add_u32 s24, s20, s23
	s_addc_u32 s25, s21, 0
	global_load_dwordx4 v[68:71], v1, s[24:25]
	s_add_u32 s23, s17, 2
	s_and_b32 s23, s23, 63
	s_lshl_b32 s23, s23, 10
	s_add_u32 s24, s20, s23
	s_addc_u32 s25, s21, 0
	global_load_dwordx4 v[72:75], v1, s[24:25]
	s_add_u32 s23, s17, 3
	s_and_b32 s23, s23, 63
	s_lshl_b32 s23, s23, 10
	s_add_u32 s24, s20, s23
	s_addc_u32 s25, s21, 0
	global_load_dwordx4 v[76:79], v1, s[24:25]
	s_add_u32 s23, s17, 4
	s_and_b32 s23, s23, 63
	s_lshl_b32 s23, s23, 10
	s_add_u32 s24, s20, s23
	s_addc_u32 s25, s21, 0
	global_load_dwordx4 v[80:83], v1, s[24:25]
	s_add_u32 s23, s17, 5
	s_and_b32 s23, s23, 63
	s_lshl_b32 s23, s23, 10
	s_add_u32 s24, s20, s23
	s_addc_u32 s25, s21, 0
	global_load_dwordx4 v[84:87], v1, s[24:25]
	s_add_u32 s23, s17, 6
	s_and_b32 s23, s23, 63
	s_lshl_b32 s23, s23, 10
	s_add_u32 s24, s20, s23
	s_addc_u32 s25, s21, 0
	global_load_dwordx4 v[88:91], v1, s[24:25]
	s_add_u32 s23, s17, 7
	s_and_b32 s23, s23, 63
	s_lshl_b32 s23, s23, 10
	s_add_u32 s24, s20, s23
	s_addc_u32 s25, s21, 0
	global_load_dwordx4 v[92:95], v1, s[24:25]
	v_mov_b32_e32 v2, 0
	v_mov_b32_e32 v3, 0
	v_mov_b32_e32 v4, 0
	v_mov_b32_e32 v5, 0
	v_mov_b32_e32 v6, 0
	v_mov_b32_e32 v7, 0
	v_mov_b32_e32 v8, 0
	v_mov_b32_e32 v9, 0
	v_mov_b32_e32 v10, 0
	v_mov_b32_e32 v11, 0
	v_mov_b32_e32 v12, 0
	v_mov_b32_e32 v13, 0
	v_mov_b32_e32 v14, 0
	v_mov_b32_e32 v15, 0
	v_mov_b32_e32 v16, 0
	v_mov_b32_e32 v17, 0
	v_mov_b32_e32 v18, 0
	v_mov_b32_e32 v19, 0
	v_mov_b32_e32 v20, 0
	v_mov_b32_e32 v21, 0
	v_mov_b32_e32 v22, 0
	v_mov_b32_e32 v23, 0
	v_mov_b32_e32 v24, 0
	v_mov_b32_e32 v25, 0
	v_mov_b32_e32 v26, 0
	v_mov_b32_e32 v27, 0
	v_mov_b32_e32 v28, 0
	v_mov_b32_e32 v29, 0
	v_mov_b32_e32 v30, 0
	v_mov_b32_e32 v31, 0
	v_mov_b32_e32 v32, 0
	v_mov_b32_e32 v33, 0
	v_mov_b32_e32 v34, 0
	v_mov_b32_e32 v35, 0
	v_mov_b32_e32 v36, 0
	v_mov_b32_e32 v37, 0
	v_mov_b32_e32 v38, 0
	v_mov_b32_e32 v39, 0
	v_mov_b32_e32 v40, 0
	v_mov_b32_e32 v41, 0
	v_lshrrev_b32_e32 v44, 1, v46
	v_subrev_u32_e32 v44, s17, v44
	v_and_b32_e32 v44, 63, v44
	v_lshlrev_b32_e32 v44, 5, v44
	v_and_b32_e32 v45, 1, v46
	v_lshl_or_b32 v44, v45, 4, v44
	v_xor_b32_e32 v45, 0x400, v44
	s_mul_i32 s23, s15, 0x1900
	s_add_u32 s23, s23, 0x11000
	v_add_u32_e32 v44, s23, v44
	v_add_u32_e32 v45, s23, v45
	v_add_u32_e32 v47, s23, v1
	ds_write_b128 v47, v[34:37] offset:4096
	ds_write_b128 v47, v[34:37] offset:5120
	s_waitcnt vmcnt(8)
	ds_write_b128 v44, v[48:51]
	ds_write_b128 v45, v[52:55]
	ds_write_b128 v44, v[56:59] offset:2048
	ds_write_b128 v45, v[60:63] offset:2048
	v_cvt_f16_f32_e32 v42, v42
	v_cvt_f16_f32_e32 v43, v43
	s_mov_b32 s28, 0x5040100
	v_perm_b32 v42, v42, v42, s28
	v_perm_b32 v43, v43, v43, s28
	v_lshrrev_b32_e32 v44, 5, v46
	v_and_b32_e32 v45, 15, v46
	v_bfe_u32 v47, v46, 4, 1
	v_cmp_eq_u32_e32 vcc, v45, v47
	v_lshlrev_b32_e32 v44, 4, v44
	v_add_u32_e32 v46, s23, v44
	v_add_u32_e32 v45, 0x800, v46
	v_mov_b32_e32 v47, s23
	v_add_u32_e32 v47, 0x1000, v47
	v_cndmask_b32_e32 v47, v47, v45, vcc
	s_waitcnt lgkmcnt(0)
	ds_read_b128 v[144:147], v46
	ds_read_b128 v[148:151], v46 offset:32
	ds_read_b128 v[160:163], v47
	ds_read_b128 v[152:155], v46 offset:64
	ds_read_b128 v[164:167], v47 offset:32
	s_add_u32 s27, s17, 8
	s_lshl_b32 s27, s27, 10
	s_add_u32 s29, s17, 63
	s_lshl_b32 s29, s29, 10
	s_movk_i32 s28, 0x400
	s_mov_b32 s26, 0
	s_waitcnt lgkmcnt(4)
	v_pk_max_u16 v128, v144, v42
	v_pk_max_u16 v129, v145, v42
	v_pk_max_u16 v130, v146, v42
	v_pk_max_u16 v131, v147, v42
	v_pk_max_u16 v136, v144, v43
	v_pk_max_u16 v137, v145, v43
	v_pk_max_u16 v138, v146, v43
	v_pk_max_u16 v139, v147, v43
	s_nop 1
.Lk2_loop:
	s_and_b32 s23, s27, 0xfc00
	s_add_u32 s24, s20, s23
	s_addc_u32 s25, s21, 0
	s_add_u32 s27, s27, s28
	s_waitcnt vmcnt(7)
	v_mfma_f32_32x32x16_f16 v[2:17], v[64:67], v[128:131], v[2:17]
	s_waitcnt lgkmcnt(3)
	v_pk_max_u16 v132, v148, v42
	v_pk_max_u16 v133, v149, v42
	v_pk_max_u16 v134, v150, v42
	v_pk_max_u16 v135, v151, v42
	v_mfma_f32_32x32x16_f16 v[18:33], v[64:67], v[136:139], v[18:33]
	v_pk_max_u16 v140, v148, v43
	v_pk_max_u16 v141, v149, v43
	v_pk_max_u16 v142, v150, v43
	v_pk_max_u16 v143, v151, v43
	s_waitcnt lgkmcnt(2)
	v_mfma_f32_16x16x32_f16 v[34:37], v[160:163], v[128:131], v[34:37]
	global_load_dwordx4 v[64:67], v1, s[24:25]
	ds_read_b128 v[156:159], v46 offset:96
	ds_read_b128 v[168:171], v47 offset:64
	v_mfma_f32_16x16x32_f16 v[38:41], v[160:163], v[136:139], v[38:41]
	s_and_b32 s23, s27, 0xfc00
	s_add_u32 s24, s20, s23
	s_addc_u32 s25, s21, 0
	s_add_u32 s27, s27, s28
	s_waitcnt vmcnt(7)
	v_mfma_f32_32x32x16_f16 v[2:17], v[68:71], v[132:135], v[2:17]
	s_waitcnt lgkmcnt(3)
	v_pk_max_u16 v128, v152, v42
	v_pk_max_u16 v129, v153, v42
	v_pk_max_u16 v130, v154, v42
	v_pk_max_u16 v131, v155, v42
	v_mfma_f32_32x32x16_f16 v[18:33], v[68:71], v[140:143], v[18:33]
	v_pk_max_u16 v136, v152, v43
	v_pk_max_u16 v137, v153, v43
	v_pk_max_u16 v138, v154, v43
	v_pk_max_u16 v139, v155, v43
	s_waitcnt lgkmcnt(2)
	v_mfma_f32_16x16x32_f16 v[34:37], v[164:167], v[132:135], v[34:37]
	global_load_dwordx4 v[68:71], v1, s[24:25]
	ds_read_b128 v[144:147], v46 offset:128
	ds_read_b128 v[172:175], v47 offset:96
	v_mfma_f32_16x16x32_f16 v[38:41], v[164:167], v[140:143], v[38:41]
	s_and_b32 s23, s27, 0xfc00
	s_add_u32 s24, s20, s23
	s_addc_u32 s25, s21, 0
	s_add_u32 s27, s27, s28
	s_waitcnt vmcnt(7)
	v_mfma_f32_32x32x16_f16 v[2:17], v[72:75], v[128:131], v[2:17]
	s_waitcnt lgkmcnt(3)
	v_pk_max_u16 v132, v156, v42
	v_pk_max_u16 v133, v157, v42
	v_pk_max_u16 v134, v158, v42
	v_pk_max_u16 v135, v159, v42
	v_mfma_f32_32x32x16_f16 v[18:33], v[72:75], v[136:139], v[18:33]
	v_pk_max_u16 v140, v156, v43
	v_pk_max_u16 v141, v157, v43
	v_pk_max_u16 v142, v158, v43
	v_pk_max_u16 v143, v159, v43
	s_waitcnt lgkmcnt(2)
	v_mfma_f32_16x16x32_f16 v[34:37], v[168:171], v[128:131], v[34:37]
	global_load_dwordx4 v[72:75], v1, s[24:25]
	ds_read_b128 v[148:151], v46 offset:160
	ds_read_b128 v[160:163], v47 offset:128
	v_mfma_f32_16x16x32_f16 v[38:41], v[168:171], v[136:139], v[38:41]
	s_and_b32 s23, s27, 0xfc00
	s_add_u32 s24, s20, s23
	s_addc_u32 s25, s21, 0
	s_add_u32 s27, s27, s28
	s_waitcnt vmcnt(7)
	v_mfma_f32_32x32x16_f16 v[2:17], v[76:79], v[132:135], v[2:17]
	s_waitcnt lgkmcnt(3)
	v_pk_max_u16 v128, v144, v42
	v_pk_max_u16 v129, v145, v42
	v_pk_max_u16 v130, v146, v42
	v_pk_max_u16 v131, v147, v42
	v_mfma_f32_32x32x16_f16 v[18:33], v[76:79], v[140:143], v[18:33]
	v_pk_max_u16 v136, v144, v43
	v_pk_max_u16 v137, v145, v43
	v_pk_max_u16 v138, v146, v43
	v_pk_max_u16 v139, v147, v43
	s_waitcnt lgkmcnt(2)
	v_mfma_f32_16x16x32_f16 v[34:37], v[172:175], v[132:135], v[34:37]
	global_load_dwordx4 v[76:79], v1, s[24:25]
	ds_read_b128 v[152:155], v46 offset:192
	ds_read_b128 v[164:167], v47 offset:160
	v_mfma_f32_16x16x32_f16 v[38:41], v[172:175], v[140:143], v[38:41]
	s_and_b32 s23, s27, 0xfc00
	s_add_u32 s24, s20, s23
	s_addc_u32 s25, s21, 0
	s_add_u32 s27, s27, s28
	s_waitcnt vmcnt(7)
	v_mfma_f32_32x32x16_f16 v[2:17], v[80:83], v[128:131], v[2:17]
	s_waitcnt lgkmcnt(3)
	v_pk_max_u16 v132, v148, v42
	v_pk_max_u16 v133, v149, v42
	v_pk_max_u16 v134, v150, v42
	v_pk_max_u16 v135, v151, v42
	v_mfma_f32_32x32x16_f16 v[18:33], v[80:83], v[136:139], v[18:33]
	v_pk_max_u16 v140, v148, v43
	v_pk_max_u16 v141, v149, v43
	v_pk_max_u16 v142, v150, v43
	v_pk_max_u16 v143, v151, v43
	s_waitcnt lgkmcnt(2)
	v_mfma_f32_16x16x32_f16 v[34:37], v[160:163], v[128:131], v[34:37]
	global_load_dwordx4 v[80:83], v1, s[24:25]
	ds_read_b128 v[156:159], v46 offset:224
	ds_read_b128 v[168:171], v47 offset:192
	v_mfma_f32_16x16x32_f16 v[38:41], v[160:163], v[136:139], v[38:41]
	s_and_b32 s23, s27, 0xfc00
	s_add_u32 s24, s20, s23
	s_addc_u32 s25, s21, 0
	s_add_u32 s27, s27, s28
	s_waitcnt vmcnt(7)
	v_mfma_f32_32x32x16_f16 v[2:17], v[84:87], v[132:135], v[2:17]
	s_waitcnt lgkmcnt(3)
	v_pk_max_u16 v128, v152, v42
	v_pk_max_u16 v129, v153, v42
	v_pk_max_u16 v130, v154, v42
	v_pk_max_u16 v131, v155, v42
	v_mfma_f32_32x32x16_f16 v[18:33], v[84:87], v[140:143], v[18:33]
	v_pk_max_u16 v136, v152, v43
	v_pk_max_u16 v137, v153, v43
	v_pk_max_u16 v138, v154, v43
	v_pk_max_u16 v139, v155, v43
	s_waitcnt lgkmcnt(2)
	v_mfma_f32_16x16x32_f16 v[34:37], v[164:167], v[132:135], v[34:37]
	global_load_dwordx4 v[84:87], v1, s[24:25]
	ds_read_b128 v[144:147], v46 offset:256
	ds_read_b128 v[172:175], v47 offset:224
	v_mfma_f32_16x16x32_f16 v[38:41], v[164:167], v[140:143], v[38:41]
	s_and_b32 s23, s27, 0xfc00
	s_add_u32 s24, s20, s23
	s_addc_u32 s25, s21, 0
	s_add_u32 s27, s27, s28
	s_waitcnt vmcnt(7)
	v_mfma_f32_32x32x16_f16 v[2:17], v[88:91], v[128:131], v[2:17]
	s_waitcnt lgkmcnt(3)
	v_pk_max_u16 v132, v156, v42
	v_pk_max_u16 v133, v157, v42
	v_pk_max_u16 v134, v158, v42
	v_pk_max_u16 v135, v159, v42
	v_mfma_f32_32x32x16_f16 v[18:33], v[88:91], v[136:139], v[18:33]
	v_pk_max_u16 v140, v156, v43
	v_pk_max_u16 v141, v157, v43
	v_pk_max_u16 v142, v158, v43
	v_pk_max_u16 v143, v159, v43
	s_waitcnt lgkmcnt(2)
	v_mfma_f32_16x16x32_f16 v[34:37], v[168:171], v[128:131], v[34:37]
	global_load_dwordx4 v[88:91], v1, s[24:25]
	ds_read_b128 v[148:151], v46 offset:288
	ds_read_b128 v[160:163], v47 offset:256
	v_mfma_f32_16x16x32_f16 v[38:41], v[168:171], v[136:139], v[38:41]
	s_and_b32 s23, s27, 0xfc00
	s_add_u32 s24, s20, s23
	s_addc_u32 s25, s21, 0
	s_add_u32 s27, s27, s28
	s_waitcnt vmcnt(7)
	v_mfma_f32_32x32x16_f16 v[2:17], v[92:95], v[132:135], v[2:17]
	s_waitcnt lgkmcnt(3)
	v_pk_max_u16 v128, v144, v42
	v_pk_max_u16 v129, v145, v42
	v_pk_max_u16 v130, v146, v42
	v_pk_max_u16 v131, v147, v42
	v_mfma_f32_32x32x16_f16 v[18:33], v[92:95], v[140:143], v[18:33]
	v_pk_max_u16 v136, v144, v43
	v_pk_max_u16 v137, v145, v43
	v_pk_max_u16 v138, v146, v43
	v_pk_max_u16 v139, v147, v43
	s_waitcnt lgkmcnt(2)
	v_mfma_f32_16x16x32_f16 v[34:37], v[172:175], v[132:135], v[34:37]
	global_load_dwordx4 v[92:95], v1, s[24:25]
	ds_read_b128 v[152:155], v46 offset:320
	ds_read_b128 v[164:167], v47 offset:288
	v_mfma_f32_16x16x32_f16 v[38:41], v[172:175], v[140:143], v[38:41]
	s_add_u32 s26, s26, 1
	v_add_u32_e32 v46, 256, v46
	v_add_u32_e32 v47, 256, v47
	s_cmp_eq_u32 s26, 7
	s_cselect_b32 s27, s29, s27
	s_cselect_b32 s28, 0, s28
	s_cmp_lt_u32 s26, 8
	s_cbranch_scc1 .Lk2_loop
	v_and_b32_e32 v180, 63, v0
	v_lshrrev_b32_e32 v181, 5, v180
	v_and_b32_e32 v182, 31, v0
	s_lshl_b32 s23, s15, 4
	v_add_u32_e32 v181, s23, v181
	v_mul_u32_u24_e32 v181, 0x210, v181
	v_lshl_add_u32 v181, v182, 4, v181
	v_cmp_gt_u32_e32 vcc, 16, v180
	ds_write_b128 v181, v[2:5]
	ds_write_b128 v181, v[18:21] offset:4224
	ds_write_b128 v181, v[6:9] offset:1056
	ds_write_b128 v181, v[22:25] offset:5280
	ds_write_b128 v181, v[10:13] offset:2112
	ds_write_b128 v181, v[26:29] offset:6336
	ds_write_b128 v181, v[14:17] offset:3168
	ds_write_b128 v181, v[30:33] offset:7392
	s_and_saveexec_b64 s[2:3], vcc
	s_cbranch_execz .Lk2_nodred
	v_lshlrev_b32_e32 v183, 2, v180
	s_lshl_b32 s23, s15, 8
	v_add_u32_e32 v183, s23, v183
	v_add_u32_e32 v183, 0x10800, v183
	ds_write2_b32 v183, v34, v35 offset1:16
	ds_write2_b32 v183, v38, v39 offset0:32 offset1:48
.Lk2_nodred:
	s_or_b64 exec, exec, s[2:3]
	v_lshrrev_b32_e32 v184, 3, v0
	v_and_b32_e32 v185, 7, v0
	v_lshrrev_b32_e32 v186, 8, v0
	v_bfe_u32 v187, v0, 3, 5
	v_lshlrev_b32_e32 v188, 2, v187
	v_lshl_or_b32 v188, v186, 7, v188
	v_add_u32_e32 v188, 0x10800, v188
	v_mul_u32_u24_e32 v189, 0x1080, v186
	v_mul_u32_u24_e32 v190, 0x210, v185
	v_lshlrev_b32_e32 v191, 4, v187
	v_add3_u32 v189, v189, v190, v191
	s_lshl_b32 s4, s18, 6
	v_or_b32_e32 v192, s4, v184
	v_mov_b32_e32 v193, 0
	v_lshlrev_b64 v[194:195], 8, v[192:193]
	v_lshl_add_u64 v[194:195], s[12:13], 0, v[194:195]
	s_lshl_b32 s2, s16, 7
	s_mov_b32 s3, 0
	v_lshl_add_u64 v[194:195], v[194:195], 0, s[2:3]
	v_lshlrev_b32_e32 v192, 4, v185
	v_lshl_add_u64 v[194:195], v[194:195], 0, v[192:193]
	s_waitcnt lgkmcnt(0)
	s_barrier
	ds_read_b128 v[196:199], v189
	ds_read_b128 v[200:203], v189 offset:8448
	ds_read_b128 v[204:207], v189 offset:16896
	ds_read_b128 v[208:211], v189 offset:25344
	ds_read_b128 v[212:215], v189 offset:33792
	ds_read_b128 v[216:219], v189 offset:42240
	ds_read_b128 v[220:223], v189 offset:50688
	ds_read_b128 v[224:227], v189 offset:59136
	ds_read_b32 v228, v188
	ds_read_b32 v229, v188 offset:256
	ds_read_b32 v230, v188 offset:512
	ds_read_b32 v231, v188 offset:768
	ds_read_b32 v232, v188 offset:1024
	ds_read_b32 v233, v188 offset:1280
	ds_read_b32 v234, v188 offset:1536
	s_waitcnt lgkmcnt(13)
	ds_read_b32 v235, v188 offset:1792
	v_pk_add_f32 v[238:239], v[198:199], v[202:203]
	v_pk_add_f32 v[236:237], v[196:197], v[200:201]
	s_waitcnt lgkmcnt(13)
	v_pk_add_f32 v[238:239], v[238:239], v[206:207]
	v_pk_add_f32 v[236:237], v[236:237], v[204:205]
	s_waitcnt lgkmcnt(12)
	v_pk_add_f32 v[238:239], v[238:239], v[210:211]
	v_pk_add_f32 v[236:237], v[236:237], v[208:209]
	s_waitcnt lgkmcnt(11)
	v_pk_add_f32 v[238:239], v[238:239], v[214:215]
	v_pk_add_f32 v[236:237], v[236:237], v[212:213]
	s_waitcnt lgkmcnt(10)
	v_pk_add_f32 v[238:239], v[238:239], v[218:219]
	v_pk_add_f32 v[236:237], v[236:237], v[216:217]
	s_waitcnt lgkmcnt(9)
	v_pk_add_f32 v[238:239], v[238:239], v[222:223]
	v_pk_add_f32 v[236:237], v[236:237], v[220:221]
	s_waitcnt lgkmcnt(8)
	v_pk_add_f32 v[238:239], v[238:239], v[226:227]
	v_pk_add_f32 v[236:237], v[236:237], v[224:225]
	s_waitcnt lgkmcnt(6)
	v_add_f32_e32 v180, v228, v229
	s_waitcnt lgkmcnt(5)
	v_add_f32_e32 v180, v180, v230
	s_waitcnt lgkmcnt(4)
	v_add_f32_e32 v180, v180, v231
	s_waitcnt lgkmcnt(3)
	v_add_f32_e32 v180, v180, v232
	s_waitcnt lgkmcnt(2)
	v_add_f32_e32 v180, v180, v233
	s_waitcnt lgkmcnt(1)
	v_add_f32_e32 v180, v180, v234
	s_waitcnt lgkmcnt(0)
	v_add_f32_e32 v180, v180, v235
	v_div_scale_f32 v181, s[2:3], v180, v180, 1.0
	v_rcp_f32_e32 v182, v181
	v_div_scale_f32 v183, vcc, 1.0, v180, 1.0
	v_fma_f32 v184, -v181, v182, 1.0
	v_fmac_f32_e32 v182, v184, v182
	v_mul_f32_e32 v184, v183, v182
	v_fma_f32 v185, -v181, v184, v183
	v_fmac_f32_e32 v184, v185, v182
	v_fma_f32 v181, -v181, v184, v183
	v_div_fmas_f32 v181, v181, v182, v184
	v_div_fixup_f32 v186, v181, v180, 1.0
	v_pk_mul_f32 v[238:239], v[238:239], v[186:187] op_sel_hi:[1,0]
	v_pk_mul_f32 v[236:237], v[236:237], v[186:187] op_sel_hi:[1,0]
	global_store_dwordx4 v[194:195], v[236:239], off
	s_endpgm

	.amdhsa_kernel _Z6gat_k2PKDF16_S0_S0_PKfPf
		.amdhsa_group_segment_fixed_size 120832
		.amdhsa_private_segment_fixed_size 0
		.amdhsa_kernarg_size 40
		.amdhsa_user_sgpr_count 2
		.amdhsa_user_sgpr_dispatch_ptr 0
		.amdhsa_user_sgpr_queue_ptr 0
		.amdhsa_user_sgpr_kernarg_segment_ptr 1
		.amdhsa_user_sgpr_dispatch_id 0
		.amdhsa_user_sgpr_kernarg_preload_length 0
		.amdhsa_user_sgpr_kernarg_preload_offset 0
		.amdhsa_user_sgpr_private_segment_size 0
		.amdhsa_uses_dynamic_stack 0
		.amdhsa_enable_private_segment 0
		.amdhsa_system_sgpr_workgroup_id_x 1
		.amdhsa_system_sgpr_workgroup_id_y 0
		.amdhsa_system_sgpr_workgroup_id_z 0
		.amdhsa_system_sgpr_workgroup_info 0
		.amdhsa_system_vgpr_workitem_id 0
		.amdhsa_next_free_vgpr 240
		.amdhsa_next_free_sgpr 96
		.amdhsa_accum_offset 240
		.amdhsa_reserve_vcc 1
		.amdhsa_float_round_mode_32 0
		.amdhsa_float_round_mode_16_64 0
		.amdhsa_float_denorm_mode_32 3
		.amdhsa_float_denorm_mode_16_64 3
		.amdhsa_dx10_clamp 1
		.amdhsa_ieee_mode 1
		.amdhsa_fp16_overflow 0
		.amdhsa_tg_split 0
		.amdhsa_exception_fp_ieee_invalid_op 0
		.amdhsa_exception_fp_denorm_src 0
		.amdhsa_exception_fp_ieee_div_zero 0
		.amdhsa_exception_fp_ieee_overflow 0
		.amdhsa_exception_fp_ieee_underflow 0
		.amdhsa_exception_fp_ieee_inexact 0
		.amdhsa_exception_int_div_zero 0
	.end_amdhsa_kernel

amdhsa.kernels:
  - .agpr_count:     32
    .args:
      - .actual_access:  read_only
        .address_space:  global
        .offset:         0
        .size:           8
        .value_kind:     global_buffer
      - .actual_access:  read_only
        .address_space:  global
        .offset:         8
        .size:           8
        .value_kind:     global_buffer
      - .actual_access:  read_only
        .address_space:  global
        .offset:         16
        .size:           8
        .value_kind:     global_buffer
      - .actual_access:  read_only
        .address_space:  global
        .offset:         24
        .size:           8
        .value_kind:     global_buffer
      - .actual_access:  write_only
        .address_space:  global
        .offset:         32
        .size:           8
        .value_kind:     global_buffer
      - .actual_access:  write_only
        .address_space:  global
        .offset:         40
        .size:           8
        .value_kind:     global_buffer
      - .actual_access:  write_only
        .address_space:  global
        .offset:         48
        .size:           8
        .value_kind:     global_buffer
      - .actual_access:  write_only
        .address_space:  global
        .offset:         56
        .size:           8
        .value_kind:     global_buffer
    .group_segment_fixed_size: 68352
    .kernarg_segment_align: 8
    .kernarg_segment_size: 64
    .language:       OpenCL C
    .language_version:
      - 2
      - 0
    .max_flat_workgroup_size: 256
    .name:           _Z6gat_k1PKfS0_S0_S0_PDF16_S1_S1_Pf
    .private_segment_fixed_size: 0
    .sgpr_count:     18
    .sgpr_spill_count: 0
    .symbol:         _Z6gat_k1PKfS0_S0_S0_PDF16_S1_S1_Pf.kd
    .uniform_work_group_size: 1
    .uses_dynamic_stack: false
    .vgpr_count:     156
    .vgpr_spill_count: 0
    .wavefront_size: 64
  - .agpr_count:     0
    .args:
      - .actual_access:  read_only
        .address_space:  global
        .offset:         0
        .size:           8
        .value_kind:     global_buffer
      - .actual_access:  read_only
        .address_space:  global
        .offset:         8
        .size:           8
        .value_kind:     global_buffer
      - .actual_access:  read_only
        .address_space:  global
        .offset:         16
        .size:           8
        .value_kind:     global_buffer
      - .actual_access:  read_only
        .address_space:  global
        .offset:         24
        .size:           8
        .value_kind:     global_buffer
      - .actual_access:  write_only
        .address_space:  global
        .offset:         32
        .size:           8
        .value_kind:     global_buffer
    .group_segment_fixed_size: 120832
    .kernarg_segment_align: 8
    .kernarg_segment_size: 40
    .language:       OpenCL C
    .language_version:
      - 2
      - 0
    .max_flat_workgroup_size: 512
    .name:           _Z6gat_k2PKDF16_S0_S0_PKfPf
    .private_segment_fixed_size: 0
    .sgpr_count:     24
    .sgpr_spill_count: 0
    .symbol:         _Z6gat_k2PKDF16_S0_S0_PKfPf.kd
    .uniform_work_group_size: 1
    .uses_dynamic_stack: false
    .vgpr_count:     240
    .vgpr_spill_count: 0
    .wavefront_size: 64
